# speedup vs baseline: 1.0049x; 1.0049x over previous
.LBB3_25:
	s_waitcnt vmcnt(7) lgkmcnt(3)
	v_mfma_f32_32x32x16_f16 v[18:33], v[34:37], v[114:117], v[18:33]
	s_waitcnt lgkmcnt(2)
	v_mfma_f32_32x32x16_f16 v[2:17], v[34:37], v[110:113], v[2:17]
	global_load_dwordx4 v[34:37], v[98:99], off
	ds_read_b128 v[110:113], v203
	ds_read_b128 v[114:117], v203 offset:33280
	s_waitcnt vmcnt(7) lgkmcnt(3)
	v_mfma_f32_32x32x16_f16 v[18:33], v[38:41], v[106:109], v[18:33]
	s_waitcnt lgkmcnt(2)
	v_mfma_f32_32x32x16_f16 v[2:17], v[38:41], v[102:105], v[2:17]
	global_load_dwordx4 v[38:41], v[98:99], off offset:1024
	ds_read_b128 v[100:103], v203 offset:32
	ds_read_b128 v[104:107], v203 offset:33312
	s_waitcnt vmcnt(7) lgkmcnt(3)
	v_mfma_f32_32x32x16_f16 v[18:33], v[42:45], v[110:113], v[18:33]
	s_waitcnt lgkmcnt(2)
	v_mfma_f32_32x32x16_f16 v[2:17], v[42:45], v[114:117], v[2:17]
	global_load_dwordx4 v[42:45], v[98:99], off offset:2048
	ds_read_b128 v[108:111], v203 offset:64
	ds_read_b128 v[112:115], v203 offset:33344
	s_waitcnt vmcnt(7) lgkmcnt(3)
	v_mfma_f32_32x32x16_f16 v[18:33], v[46:49], v[100:103], v[18:33]
	s_waitcnt lgkmcnt(2)
	v_mfma_f32_32x32x16_f16 v[2:17], v[46:49], v[104:107], v[2:17]
	global_load_dwordx4 v[46:49], v[98:99], off offset:3072
	ds_read_b128 v[100:103], v203 offset:96
	ds_read_b128 v[104:107], v203 offset:33376
	s_waitcnt vmcnt(7) lgkmcnt(3)
	v_mfma_f32_32x32x16_f16 v[18:33], v[54:57], v[108:111], v[18:33]
	v_add_co_u32_e32 v108, vcc, s9, v98
	v_lshl_add_u64 v[118:119], v[98:99], 0, s[6:7]
	s_nop 0
	v_addc_co_u32_e32 v109, vcc, 0, v99, vcc
	s_waitcnt lgkmcnt(2)
	v_mfma_f32_32x32x16_f16 v[2:17], v[54:57], v[112:115], v[2:17]
	global_load_dwordx4 v[54:57], v[108:109], off
	ds_read_b128 v[108:111], v203 offset:128
	ds_read_b128 v[112:115], v203 offset:33408
	s_waitcnt vmcnt(7) lgkmcnt(3)
	v_mfma_f32_32x32x16_f16 v[18:33], v[50:53], v[100:103], v[18:33]
	s_waitcnt lgkmcnt(2)
	v_mfma_f32_32x32x16_f16 v[2:17], v[50:53], v[104:107], v[2:17]
	global_load_dwordx4 v[50:53], v[118:119], off offset:1024
	ds_read_b128 v[100:103], v203 offset:160
	ds_read_b128 v[104:107], v203 offset:33440
	s_waitcnt vmcnt(7) lgkmcnt(3)
	v_mfma_f32_32x32x16_f16 v[18:33], v[58:61], v[108:111], v[18:33]
	s_waitcnt lgkmcnt(2)
	v_mfma_f32_32x32x16_f16 v[2:17], v[58:61], v[112:115], v[2:17]
	global_load_dwordx4 v[58:61], v[118:119], off offset:2048
	ds_read_b128 v[114:117], v203 offset:192
	ds_read_b128 v[110:113], v203 offset:33472
	s_waitcnt vmcnt(7) lgkmcnt(3)
	v_mfma_f32_32x32x16_f16 v[18:33], v[62:65], v[100:103], v[18:33]
	s_waitcnt lgkmcnt(2)
	v_mfma_f32_32x32x16_f16 v[2:17], v[62:65], v[104:107], v[2:17]
	global_load_dwordx4 v[62:65], v[118:119], off offset:3072
	ds_read_b128 v[106:109], v203 offset:224
	ds_read_b128 v[102:105], v203 offset:33504
	s_add_i32 s3, s3, 8
	s_cmp_lt_u32 s3, 16
	v_add_u32_e32 v203, 0x100, v203
	v_lshl_add_u64 v[98:99], v[98:99], 0, s[0:1]
	s_cbranch_scc1 .LBB3_25
	v_add_u32_e32 v118, v189, v150
	s_waitcnt vmcnt(7) lgkmcnt(3)
	v_mfma_f32_32x32x16_f16 v[18:33], v[34:37], v[114:117], v[18:33]
	ds_read_b128 v[98:101], v118 offset:832
	ds_read_b128 v[114:117], v118 offset:34112
	s_waitcnt lgkmcnt(4)
	v_mfma_f32_32x32x16_f16 v[2:17], v[34:37], v[110:113], v[2:17]
	s_waitcnt vmcnt(6) lgkmcnt(3)
	v_mfma_f32_32x32x16_f16 v[18:33], v[38:41], v[106:109], v[18:33]
	ds_read_b128 v[34:37], v118 offset:864
	ds_read_b128 v[106:109], v118 offset:34144
	s_waitcnt lgkmcnt(4)
	v_mfma_f32_32x32x16_f16 v[2:17], v[38:41], v[102:105], v[2:17]
	s_waitcnt vmcnt(5) lgkmcnt(3)
	v_mfma_f32_32x32x16_f16 v[18:33], v[42:45], v[98:101], v[18:33]
	ds_read_b128 v[38:41], v118 offset:896
	ds_read_b128 v[98:101], v118 offset:34176
	s_waitcnt lgkmcnt(4)
	v_mfma_f32_32x32x16_f16 v[2:17], v[42:45], v[114:117], v[2:17]
	s_waitcnt vmcnt(4) lgkmcnt(3)
	v_mfma_f32_32x32x16_f16 v[18:33], v[46:49], v[34:37], v[18:33]
	ds_read_b128 v[34:37], v118 offset:928
	ds_read_b128 v[42:45], v118 offset:34208
	s_waitcnt lgkmcnt(4)
	v_mfma_f32_32x32x16_f16 v[2:17], v[46:49], v[106:109], v[2:17]
	s_waitcnt vmcnt(3) lgkmcnt(3)
	v_mfma_f32_32x32x16_f16 v[18:33], v[54:57], v[38:41], v[18:33]
	ds_read_b128 v[38:41], v118 offset:960
	ds_read_b128 v[46:49], v118 offset:34240
	s_waitcnt lgkmcnt(4)
	v_mfma_f32_32x32x16_f16 v[2:17], v[54:57], v[98:101], v[2:17]
	s_waitcnt vmcnt(2) lgkmcnt(3)
	v_mfma_f32_32x32x16_f16 v[18:33], v[50:53], v[34:37], v[18:33]
	ds_read_b128 v[34:37], v118 offset:992
	ds_read_b128 v[54:57], v118 offset:34272
	s_waitcnt lgkmcnt(4)
	v_mfma_f32_32x32x16_f16 v[2:17], v[50:53], v[42:45], v[2:17]
	s_waitcnt vmcnt(1) lgkmcnt(3)
	v_mfma_f32_32x32x16_f16 v[18:33], v[58:61], v[38:41], v[18:33]
	s_waitcnt lgkmcnt(2)
	v_mfma_f32_32x32x16_f16 v[2:17], v[58:61], v[46:49], v[2:17]
	s_waitcnt vmcnt(0) lgkmcnt(1)
	v_mfma_f32_32x32x16_f16 v[18:33], v[62:65], v[34:37], v[18:33]
	s_waitcnt lgkmcnt(0)
	v_mfma_f32_32x32x16_f16 v[2:17], v[62:65], v[54:57], v[2:17]
	v_lshlrev_b32_e32 v38, 2, v191
	s_add_i32 s0, 0, 0x13000
	v_add_u32_e32 v52, s0, v38
	ds_read_b128 v[34:37], v52
	v_lshl_add_u32 v52, v194, 2, s0
	ds_read_b128 v[40:43], v52
	v_lshl_add_u32 v52, v200, 2, s0
	ds_read_b128 v[44:47], v52
	v_lshl_add_u32 v52, v201, 2, s0
	ds_read_b128 v[48:51], v52
	v_add3_u32 v38, 0, v38, v187
	s_and_b32 s5, s5, 0xffff
	s_mov_b32 s7, 0x20000
	s_mov_b32 s6, 0x1000000
	s_waitcnt lgkmcnt(0)
	s_barrier
	v_pk_add_f32 v[18:19], v[34:35], v[18:19]
	v_pk_add_f32 v[20:21], v[36:37], v[20:21]
	v_pk_add_f32 v[2:3], v[34:35], v[2:3]
	v_pk_add_f32 v[4:5], v[36:37], v[4:5]
	ds_write_b128 v38, v[18:21]
	ds_write_b128 v38, v[2:5] offset:33280
	v_pk_add_f32 v[22:23], v[40:41], v[22:23]
	v_pk_add_f32 v[24:25], v[42:43], v[24:25]
	v_pk_add_f32 v[6:7], v[40:41], v[6:7]
	v_pk_add_f32 v[8:9], v[42:43], v[8:9]
	ds_write_b128 v38, v[22:25] offset:32
	ds_write_b128 v38, v[6:9] offset:33312
	v_pk_add_f32 v[26:27], v[44:45], v[26:27]
	v_pk_add_f32 v[28:29], v[46:47], v[28:29]
	v_pk_add_f32 v[10:11], v[44:45], v[10:11]
	v_pk_add_f32 v[12:13], v[46:47], v[12:13]
	ds_write_b128 v38, v[26:29] offset:64
	ds_write_b128 v38, v[10:13] offset:33344
	v_pk_add_f32 v[30:31], v[48:49], v[30:31]
	v_pk_add_f32 v[32:33], v[50:51], v[32:33]
	v_pk_add_f32 v[14:15], v[48:49], v[14:15]
	v_pk_add_f32 v[16:17], v[50:51], v[16:17]
	ds_write_b128 v38, v[30:33] offset:96
	ds_write_b128 v38, v[14:17] offset:33376
	v_lshl_add_u32 v10, v188, 2, 0
	s_lshl_b32 s0, s2, 16
	v_lshl_or_b32 v0, v0, 4, s0
	v_add_u32_e32 v2, v10, v199
	s_waitcnt lgkmcnt(0)
	s_barrier
	ds_read_b128 v[2:5], v2
	v_add_u32_e32 v6, v10, v198
	ds_read_b128 v[6:9], v6
	s_waitcnt lgkmcnt(1)
	v_pk_add_f32 v[4:5], v[4:5], v[92:93]
	v_pk_add_f32 v[2:3], v[2:3], v[90:91]
	buffer_store_dwordx4 v[2:5], v0, s[4:7], 0 offen sc1
	v_add_u32_e32 v0, v10, v197
	s_waitcnt lgkmcnt(0)
	v_pk_add_f32 v[4:5], v[8:9], v[96:97]
	v_pk_add_f32 v[2:3], v[6:7], v[94:95]
	ds_read_b128 v[6:9], v0
	v_lshl_or_b32 v0, v186, 4, s0
	buffer_store_dwordx4 v[2:5], v0, s[4:7], 0 offen sc1
	v_add_u32_e32 v0, v10, v195
	ds_read_b128 v[2:5], v0
	s_waitcnt lgkmcnt(1)
	v_pk_add_f32 v[8:9], v[8:9], v[88:89]
	v_pk_add_f32 v[6:7], v[6:7], v[86:87]
	v_lshl_or_b32 v0, v182, 4, s0
	buffer_store_dwordx4 v[6:9], v0, s[4:7], 0 offen sc1
	v_add_u32_e32 v0, v10, v196
	s_waitcnt lgkmcnt(0)
	v_pk_add_f32 v[4:5], v[4:5], v[84:85]
	v_pk_add_f32 v[2:3], v[2:3], v[82:83]
	ds_read_b128 v[6:9], v0
	v_lshl_or_b32 v0, v185, 4, s0
	buffer_store_dwordx4 v[2:5], v0, s[4:7], 0 offen sc1
	v_add_u32_e32 v0, v10, v193
	ds_read_b128 v[2:5], v0
	s_waitcnt lgkmcnt(1)
	v_pk_add_f32 v[8:9], v[8:9], v[80:81]
	v_pk_add_f32 v[6:7], v[6:7], v[78:79]
	v_lshl_or_b32 v0, v179, 4, s0
	buffer_store_dwordx4 v[6:9], v0, s[4:7], 0 offen sc1
	v_add_u32_e32 v0, v10, v192
	s_waitcnt lgkmcnt(0)
	v_pk_add_f32 v[4:5], v[4:5], v[76:77]
	v_pk_add_f32 v[2:3], v[2:3], v[74:75]
	ds_read_b128 v[6:9], v0
	v_lshl_or_b32 v0, v184, 4, s0
	buffer_store_dwordx4 v[2:5], v0, s[4:7], 0 offen sc1
	v_add_u32_e32 v0, v10, v190
	ds_read_b128 v[2:5], v0
	s_waitcnt lgkmcnt(1)
	v_pk_add_f32 v[8:9], v[8:9], v[72:73]
	v_pk_add_f32 v[6:7], v[6:7], v[70:71]
	v_lshl_or_b32 v0, v1, 4, s0
	buffer_store_dwordx4 v[6:9], v0, s[4:7], 0 offen sc1
	s_waitcnt lgkmcnt(0)
	v_pk_add_f32 v[4:5], v[4:5], v[68:69]
	v_pk_add_f32 v[2:3], v[2:3], v[66:67]
	v_lshl_or_b32 v0, v183, 4, s0
	buffer_store_dwordx4 v[2:5], v0, s[4:7], 0 offen sc1
	s_endpgm
